# v13 + last 5760 layer-0 expert-weight copy items moved from the prologue to idle waves 3..7 of the layer-0 router phase
# speedup vs baseline: 1.0044x; 1.0005x over previous
; #define LAS __attribute__((address_space(3)))
; template <class T> __device__ __forceinline__ T* wsp(const Frame& F, size_t off) { return (T*)(F.ws + off); }
;     LAS float* scr = (LAS float*)(F.lds + RING_OFF + F.wave * 16384);
;     const int gw = (ncu ? (int)blockIdx.x - cu0 : F.vcu) * NWAVES + F.wave, NGW = (ncu ? ncu : F.G) * NWAVES;
;     bf16* UP = wsp<bf16>(F, WS_WEUP); bf16* DN = wsp<bf16>(F, WS_WEDN);
;     for (int it = it0 + gw; it < it1; it += NGW) {
;         const int e = it / 384, r = it % 384; const size_t eo = (size_t)(layer * 64 + e) * 1024 * 256;
;         if (r < 128) p0_transpose_item(inp(F, I_WGATE) + eo, 1024, 256, UP + (size_t)e * 512 * 1024, 3, scr, r, F.lane);
;         else if (r < 256) p0_transpose_item(inp(F, I_WUP) + eo, 1024, 256, UP + (size_t)e * 512 * 1024, 4, scr, r - 128, F.lane);
;         else p0_transpose_item(inp(F, I_WDOWN) + eo, 256, 1024, DN + (size_t)e * 1024 * 256, 5, scr, r - 256, F.lane, 16.f);
;     }
; }
.LBB0_121:
	s_movk_i32 s31, 0x497f
	s_and_b64 s[0:1], s[40:41], exec
	s_cselect_b32 s0, 0, 0x2400
	s_cselect_b32 s31, 0x5fff, s31
	s_add_i32 s1, s77, s0
	s_cmp_gt_i32 s1, s31
	s_cbranch_scc1 .LBB0_132
	s_add_u32 s14, s38, 0x4800000
	s_addc_u32 s15, s39, 0
	s_add_u32 s16, s38, 0x2800000
	v_readlane_b32 s92, v255, 4
	v_readlane_b32 s6, v255, 2
	v_readlane_b32 s28, v255, 0
	s_addc_u32 s17, s39, 0
	v_and_b32_e32 v1, 28, v45
	s_lshl_b32 s18, s1, 6
	s_lshl_b32 s19, s9, 6
	s_lshl_b32 s20, s1, 5
	s_lshl_b32 s21, s9, 5
	s_lshl_b32 s40, s1, 3
	s_lshl_b32 s41, s9, 3
	s_lshl_b32 s42, s1, 1
	s_lshl_b32 s43, s9, 1
	s_add_i32 s44, 0, 0x202a8
	v_mov_b32_e32 v7, 0
	s_movk_i32 s45, 0x1000
	s_movk_i32 s46, 0x2000
	s_movk_i32 s47, 0x4000
	s_movk_i32 s48, 0x6000
	s_movk_i32 s49, 0x7000
	s_mov_b32 s0, 0x41800000
	s_movk_i32 s50, 0x7fff
	s_mov_b32 s51, 0xffff0000
	s_mov_b64 s[2:3], 0x600
	s_add_i32 s52, 0, 0x202a0
	s_add_i32 s53, 0, 0x20298
	v_mov_b32_e32 v10, 1
	v_mov_b32_e32 v11, 0x400
	v_mov_b32_e32 v12, 0x7c
	v_readlane_b32 s93, v255, 5
	v_readlane_b32 s7, v255, 3
	v_readlane_b32 s29, v255, 1
	s_branch .LBB0_124
.LBB0_123:
	s_add_i32 s1, s1, s9
	s_add_i32 s18, s18, s19
	s_add_i32 s20, s20, s21
	s_add_i32 s40, s40, s41
	s_add_i32 s42, s42, s43
	s_cmp_gt_i32 s1, s31
	global_store_dwordx4 v[8:9], v[2:5], off nt
	s_cbranch_scc1 .LBB0_133

; #define LAS __attribute__((address_space(3)))
; template <class T> __device__ __forceinline__ T* wsp(const Frame& F, size_t off) { return (T*)(F.ws + off); }
;     LAS float* scr = (LAS float*)(F.lds + RING_OFF + F.wave * 16384);
;     const int gw = (ncu ? (int)blockIdx.x - cu0 : F.vcu) * NWAVES + F.wave, NGW = (ncu ? ncu : F.G) * NWAVES;
;     bf16* UP = wsp<bf16>(F, WS_WEUP); bf16* DN = wsp<bf16>(F, WS_WEDN);
;     for (int it = it0 + gw; it < it1; it += NGW) {
.Lcv0_entry:
	s_cmpk_lg_i32 s67, 0x100
	s_cbranch_scc1 .Lcv0_end
	v_mov_b32_e32 v2, v0
	s_mul_i32 s4, s71, 5
	s_movk_i32 s2, 0x500
	v_readfirstlane_b32 s5, v2
	s_movk_i32 s3, 0x2000
	s_ashr_i32 s5, s5, 6
	s_cmpk_lt_i32 s5, 3
	s_cbranch_scc1 .Lcv0_end
	s_add_i32 s5, s5, s4
	s_addk_i32 s5, 0x497d
	s_cmpk_gt_i32 s5, 0x5fff
	s_cbranch_scc1 .Lcv0_end
	s_add_u32 s9, s38, 0x4800000
	s_addc_u32 s18, s39, 0
	s_add_u32 s19, s38, 0x2800000
	v_and_b32_e32 v1, 56, v2
	v_lshlrev_b32_e32 v2, 2, v2
	s_addc_u32 s20, s39, 0
	v_and_b32_e32 v10, 28, v2
	s_lshl_b32 s21, s5, 6
	s_lshl_b32 s22, s2, 6
	s_lshl_b32 s23, s5, 5
	s_lshl_b32 s40, s2, 5
	s_lshl_b32 s41, s5, 3
	s_lshl_b32 s42, s2, 3
	s_lshl_b32 s43, s5, 1
	s_lshl_b32 s44, s2, 1
	s_add_i32 s45, 0, 0x202a8
	s_waitcnt lgkmcnt(1)
	v_mov_b32_e32 v7, 0
	s_movk_i32 s46, 0x1000
	s_movk_i32 s47, 0x4000
	s_movk_i32 s48, 0x6000
	s_movk_i32 s49, 0x7000
	s_mov_b32 s4, 0x41800000
	s_movk_i32 s50, 0x7fff
	s_mov_b32 s51, 0xffff0000
	s_mov_b64 s[10:11], 0x600
	s_add_i32 s52, 0, 0x202a0
	s_add_i32 s53, 0, 0x20298
	v_mov_b32_e32 v11, 1
	v_mov_b32_e32 v12, 0x400
	v_mov_b32_e32 v13, 0x7c
	s_branch .Lcv0_07

;     ...
;     for (int it = it0 + gw; it < it1; it += NGW) {
;         const int e = it / 384, r = it % 384; const size_t eo = (size_t)(layer * 64 + e) * 1024 * 256;
;         if (r < 128) p0_transpose_item(inp(F, I_WGATE) + eo, 1024, 256, UP + (size_t)e * 512 * 1024, 3, scr, r, F.lane);
;         else if (r < 256) p0_transpose_item(inp(F, I_WUP) + eo, 1024, 256, UP + (size_t)e * 512 * 1024, 4, scr, r - 128, F.lane);
;         else p0_transpose_item(inp(F, I_WDOWN) + eo, 256, 1024, DN + (size_t)e * 1024 * 256, 5, scr, r - 256, F.lane, 16.f);
.Lcv0_07:
	s_mul_hi_i32 s12, s5, 0x2aaaaaab
	s_lshr_b32 s13, s12, 31
	s_ashr_i32 s12, s12, 6
	s_add_i32 s12, s12, s13
	s_mul_i32 s13, s12, 0xfffffe80
	s_add_i32 s54, s5, s13
	s_ashr_i32 s13, s12, 31
	s_lshl_b64 s[14:15], s[12:13], 18
	s_add_u32 s14, s14, 0
	s_addc_u32 s15, s15, 0
	s_cmpk_gt_i32 s54, 0x7f
	s_mov_b64 s[16:17], -1
	s_cbranch_scc0 .Lcv0_13
	s_cmpk_gt_u32 s54, 0xff
	s_cbranch_scc0 .Lcv0_10
; #define GAS __attribute__((address_space(1)))
; __device__ __forceinline__ unsigned pk2(float lo, float hi) { return f2bf(lo) | (f2bf(hi) << 16); }
; #define NTLD(P) (NT_STREAMS ? __builtin_nontemporal_load(P) : *(P))
;     (void)scr;
;     const int nblk = N / 32, kb = item / nblk, nb = item % nblk, a = lane & 7, q = lane >> 3, k0 = 64 * kb + 8 * q, n0 = 32 * nb + 4 * a;
;     const GAS f32x4* src = (const GAS f32x4*)(W + (size_t)k0 * N + n0);
;     f32x4 r[8];
; #pragma unroll
;     for (int i = 0; i < 8; ++i) r[i] = NTLD(src + (size_t)i * (N / 4));
; #pragma unroll
;     for (int j = 0; j < 4; ++j) { v4u o; o.x = pk2(r[0][j] * scale, r[1][j] * scale); o.y = pk2(r[2][j] * scale, r[3][j] * scale); o.z = pk2(r[4][j] * scale, r[5][j] * scale); o.w = pk2(r[6][j] * scale, r[7][j] * scale);
;         if (NT_STREAMS) __builtin_nontemporal_store(o, (GAS v4u*)(WT + (size_t)maprow(mode, n0 + j) * K + k0)); else *(GAS v4u*)(WT + (size_t)maprow(mode, n0 + j) * K + k0) = o; }
; }
	v_mov_b32_e32 v2, s45
	ds_read_b64 v[2:3], v2
	s_lshl_b64 s[16:17], s[14:15], 2
	s_waitcnt lgkmcnt(0)
	v_readfirstlane_b32 s30, v2
	v_readfirstlane_b32 s31, v3
	s_add_u32 s16, s30, s16
	s_addc_u32 s17, s31, s17
	s_lshl_b64 s[56:57], s[12:13], 19
	s_add_u32 s56, s19, s56
	s_addc_u32 s57, s20, s57
	s_lshl_b32 s30, s12, 8
	s_sub_i32 s30, s43, s30
	s_and_b32 s30, s30, 0x1c0
	v_or_b32_e32 v42, s30, v1
	s_and_b32 s30, s23, 0x3e0
	v_or_b32_e32 v4, s30, v10
	v_lshlrev_b32_e32 v6, 12, v42
	v_lshl_add_u64 v[2:3], s[16:17], 0, v[6:7]
	v_lshlrev_b32_e32 v6, 2, v4
	v_lshl_add_u64 v[8:9], v[2:3], 0, v[6:7]
	v_add_co_u32_e32 v18, vcc, s3, v8
	global_load_dwordx4 v[2:5], v[8:9], off nt
	s_nop 0
	v_addc_co_u32_e32 v19, vcc, 0, v9, vcc
	v_add_co_u32_e32 v26, vcc, s47, v8
	global_load_dwordx4 v[14:17], v[18:19], off offset:-4096 nt
	s_nop 0
	global_load_dwordx4 v[18:21], v[18:19], off nt
	v_addc_co_u32_e32 v27, vcc, 0, v9, vcc
	v_add_co_u32_e32 v34, vcc, s48, v8
	global_load_dwordx4 v[22:25], v[26:27], off offset:-4096 nt
	s_nop 0
	global_load_dwordx4 v[26:29], v[26:27], off nt
	v_addc_co_u32_e32 v35, vcc, 0, v9, vcc
	v_add_co_u32_e32 v8, vcc, s49, v8
	global_load_dwordx4 v[30:33], v[34:35], off offset:-4096 nt
	s_nop 0
	global_load_dwordx4 v[34:37], v[34:35], off nt
	v_addc_co_u32_e32 v9, vcc, 0, v9, vcc
	global_load_dwordx4 v[38:41], v[8:9], off nt
	s_lshr_b32 s16, s54, 1
	v_lshlrev_b32_e32 v8, 1, v42
	v_and_b32_e32 v6, 0x3f0, v6
	v_mov_b32_e32 v9, v7
	v_and_or_b32 v6, s16, 12, v6
	v_lshl_add_u64 v[8:9], s[56:57], 0, v[8:9]
	v_lshlrev_b32_e32 v6, 9, v6
	v_lshl_add_u64 v[8:9], v[8:9], 0, v[6:7]
	s_mov_b64 s[16:17], 0
	s_waitcnt vmcnt(7)
	v_mov_b32_e32 v42, v2
	s_waitcnt vmcnt(6)
	v_mov_b32_e32 v44, v14
	s_waitcnt vmcnt(5)
	v_mov_b32_e32 v43, v18
	v_mov_b32_e32 v18, v3
	v_pk_mul_f32 v[2:3], v[42:43], s[4:5] op_sel_hi:[1,0]
	v_pk_mul_f32 v[18:19], v[18:19], s[4:5] op_sel_hi:[1,0]
	s_waitcnt vmcnt(4)
	v_mov_b32_e32 v45, v22
	s_waitcnt vmcnt(3)
	v_mov_b32_e32 v46, v26
	v_mov_b32_e32 v22, v15
	v_pk_mul_f32 v[14:15], v[44:45], s[4:5] op_sel_hi:[1,0]
	v_pk_mul_f32 v[22:23], v[22:23], s[4:5] op_sel_hi:[1,0]
	s_waitcnt vmcnt(2)
	v_mov_b32_e32 v48, v30
	s_waitcnt vmcnt(1)
	v_mov_b32_e32 v47, v34
	v_mov_b32_e32 v34, v27
	v_pk_mul_f32 v[26:27], v[46:47], s[4:5] op_sel_hi:[1,0]
	s_waitcnt vmcnt(0)
	v_mov_b32_e32 v49, v38
	v_mov_b32_e32 v38, v31
	v_pk_mul_f32 v[30:31], v[48:49], s[4:5] op_sel_hi:[1,0]
	v_bfe_u32 v46, v27, 16, 1
	v_bfe_u32 v47, v2, 16, 1
	v_bfe_u32 v6, v31, 16, 1
	v_bfe_u32 v44, v14, 16, 1
	v_bfe_u32 v48, v3, 16, 1
	v_add3_u32 v27, v27, v46, s50
	v_add3_u32 v2, v2, v47, s50
	v_bfe_u32 v42, v30, 16, 1
	v_bfe_u32 v43, v15, 16, 1
	v_bfe_u32 v45, v26, 16, 1
	v_add3_u32 v14, v14, v44, s50
	v_add3_u32 v6, v31, v6, s50
	v_add3_u32 v3, v3, v48, s50
	v_lshrrev_b32_e32 v27, 16, v27
	v_lshrrev_b32_e32 v2, 16, v2
	v_pk_mul_f32 v[34:35], v[34:35], s[4:5] op_sel_hi:[1,0]
	v_add3_u32 v15, v15, v43, s50
	v_add3_u32 v30, v30, v42, s50
	v_add3_u32 v26, v26, v45, s50
	v_lshrrev_b32_e32 v3, 16, v3
	v_and_or_b32 v45, v6, s51, v27
	v_and_or_b32 v42, v14, s51, v2
	v_bfe_u32 v6, v18, 16, 1
	v_bfe_u32 v14, v19, 16, 1
	v_pk_mul_f32 v[38:39], v[38:39], s[4:5] op_sel_hi:[1,0]
	v_bfe_u32 v51, v23, 16, 1
	v_bfe_u32 v52, v22, 16, 1
	v_lshrrev_b32_e32 v26, 16, v26
	v_and_or_b32 v43, v15, s51, v3
	v_bfe_u32 v2, v34, 16, 1
	v_bfe_u32 v3, v35, 16, 1
	v_add3_u32 v14, v19, v14, s50
	v_add3_u32 v6, v18, v6, s50
	v_bfe_u32 v49, v39, 16, 1
	v_bfe_u32 v50, v38, 16, 1
	v_add3_u32 v22, v22, v52, s50
	v_add3_u32 v23, v23, v51, s50
	v_and_or_b32 v44, v30, s51, v26
	v_add3_u32 v3, v35, v3, s50
	v_add3_u32 v2, v34, v2, s50
	v_lshrrev_b32_e32 v6, 16, v6
	v_lshrrev_b32_e32 v14, 16, v14
	v_add3_u32 v31, v38, v50, s50
	v_add3_u32 v38, v39, v49, s50
	global_store_dwordx4 v[8:9], v[42:45], off nt
	v_lshrrev_b32_e32 v2, 16, v2
	v_lshrrev_b32_e32 v3, 16, v3
	v_and_or_b32 v43, v23, s51, v14
	v_and_or_b32 v42, v22, s51, v6
	v_mov_b32_e32 v22, v32
	v_mov_b32_e32 v23, v40
	v_and_or_b32 v45, v38, s51, v3
	v_and_or_b32 v44, v31, s51, v2
	v_mov_b32_e32 v2, v4
	v_mov_b32_e32 v3, v20
	v_mov_b32_e32 v14, v16
	v_mov_b32_e32 v15, v24
	v_pk_mul_f32 v[22:23], v[22:23], s[4:5] op_sel_hi:[1,0]
	v_pk_mul_f32 v[2:3], v[2:3], s[4:5] op_sel_hi:[1,0]
	v_pk_mul_f32 v[14:15], v[14:15], s[4:5] op_sel_hi:[1,0]
	v_mov_b32_e32 v18, v28
	v_mov_b32_e32 v19, v36
	v_bfe_u32 v4, v23, 16, 1
	v_bfe_u32 v6, v22, 16, 1
	v_pk_mul_f32 v[18:19], v[18:19], s[4:5] op_sel_hi:[1,0]
	v_bfe_u32 v16, v15, 16, 1
	v_bfe_u32 v20, v14, 16, 1
	v_add3_u32 v6, v22, v6, s50
	v_add3_u32 v4, v23, v4, s50
	v_bfe_u32 v22, v2, 16, 1
	v_bfe_u32 v23, v3, 16, 1
	v_add3_u32 v14, v14, v20, s50
	v_add3_u32 v15, v15, v16, s50
	v_bfe_u32 v16, v18, 16, 1
	v_bfe_u32 v20, v19, 16, 1
	v_add3_u32 v3, v3, v23, s50
	v_add3_u32 v2, v2, v22, s50
	v_add3_u32 v19, v19, v20, s50
	v_add3_u32 v16, v18, v16, s50
	v_lshrrev_b32_e32 v2, 16, v2
	v_lshrrev_b32_e32 v3, 16, v3
	v_mov_b32_e32 v24, v17
	global_store_dwordx4 v[8:9], v[42:45], off offset:512 nt
	v_lshrrev_b32_e32 v16, 16, v16
	v_lshrrev_b32_e32 v18, 16, v19
	v_and_or_b32 v43, v15, s51, v3
	v_and_or_b32 v42, v14, s51, v2
	v_pk_mul_f32 v[2:3], v[24:25], s[4:5] op_sel_hi:[1,0]
	v_and_or_b32 v45, v4, s51, v18
	v_and_or_b32 v44, v6, s51, v16
	v_and_b32_sdwa v4, v3, v11 dst_sel:DWORD dst_unused:UNUSED_PAD src0_sel:WORD_1 src1_sel:DWORD
	v_and_b32_sdwa v6, v2, v11 dst_sel:DWORD dst_unused:UNUSED_PAD src0_sel:WORD_1 src1_sel:DWORD
	v_add3_u32 v3, v3, v4, s50
	v_add3_u32 v2, v2, v6, s50
	v_mov_b32_e32 v20, v5
	v_and_b32_e32 v4, 0xffff0000, v3
	v_and_b32_e32 v6, 0xffff0000, v2
	v_pk_mul_f32 v[2:3], v[20:21], s[4:5] op_sel_hi:[1,0]
	v_mov_b32_e32 v28, v33
	v_and_b32_sdwa v5, v3, v11 dst_sel:DWORD dst_unused:UNUSED_PAD src0_sel:WORD_1 src1_sel:DWORD
	v_and_b32_sdwa v14, v2, v11 dst_sel:DWORD dst_unused:UNUSED_PAD src0_sel:WORD_1 src1_sel:DWORD
	v_add3_u32 v3, v3, v5, s50
	v_add3_u32 v2, v2, v14, s50
	v_or_b32_sdwa v3, v4, v3 dst_sel:DWORD dst_unused:UNUSED_PAD src0_sel:DWORD src1_sel:WORD_1
	v_pk_mul_f32 v[4:5], v[28:29], s[4:5] op_sel_hi:[1,0]
	v_or_b32_sdwa v2, v6, v2 dst_sel:DWORD dst_unused:UNUSED_PAD src0_sel:DWORD src1_sel:WORD_1
	v_and_b32_sdwa v6, v5, v11 dst_sel:DWORD dst_unused:UNUSED_PAD src0_sel:WORD_1 src1_sel:DWORD
	v_and_b32_sdwa v14, v4, v11 dst_sel:DWORD dst_unused:UNUSED_PAD src0_sel:WORD_1 src1_sel:DWORD
	v_add3_u32 v5, v5, v6, s50
	v_mov_b32_e32 v36, v41
	v_add3_u32 v4, v4, v14, s50
	v_lshrrev_b32_e32 v5, 16, v5
	v_pk_mul_f32 v[14:15], v[36:37], s[4:5] op_sel_hi:[1,0]
	v_and_or_b32 v4, v4, s51, v5
	v_and_b32_sdwa v5, v15, v11 dst_sel:DWORD dst_unused:UNUSED_PAD src0_sel:WORD_1 src1_sel:DWORD
	v_and_b32_sdwa v6, v14, v11 dst_sel:DWORD dst_unused:UNUSED_PAD src0_sel:WORD_1 src1_sel:DWORD
	v_add3_u32 v5, v15, v5, s50
	v_add3_u32 v6, v14, v6, s50
	v_lshrrev_b32_e32 v5, 16, v5
	global_store_dwordx4 v[8:9], v[42:45], off offset:1024 nt
	v_and_or_b32 v5, v6, s51, v5
	v_lshl_add_u64 v[8:9], v[8:9], 0, s[10:11]

;     __device__ __forceinline__ void st(const void* p, const u32x4& v) const { __builtin_amdgcn_raw_buffer_store_b128(v, r, (unsigned)((const unsigned char*)p - b), 0, EPI_SC1); }
; __device__ __forceinline__ unsigned xb_ld(unsigned* p)              { return __hip_atomic_load(p, __ATOMIC_RELAXED, __HIP_MEMORY_SCOPE_AGENT); }
; __device__ __forceinline__ void xcd_barrier_complete(unsigned* bar, unsigned x, unsigned& nloc, unsigned& nx) {
;     const unsigned G = gridDim.x * gridDim.y * gridDim.z;
;     unsigned sum, cnt, mine, sp = 0u;
;     for (;;) {
;         sum = 0u; cnt = 0u; mine = 0u;
; #pragma unroll
;         for (unsigned j = 0; j < 16; ++j) { const unsigned c = xb_ld(&bar[XB_XCNT(j)]); sum += c; cnt += (c > 0u) ? 1u : 0u; mine = (j == x) ? c : mine; }
; __device__ __forceinline__ void xcd_barrier(const XcdBarrier& b) {
;     asm volatile("s_waitcnt vmcnt(0)" ::: "memory");
;     __syncthreads();
;     if (threadIdx.x == 0) {
;         unsigned* bar = b.bar;
;         __builtin_amdgcn_s_waitcnt(0);
;         unsigned nloc = b.st[0], nx = b.st[1];
;         if (nloc == 0u) { xcd_barrier_complete(bar, b.x, nloc, nx); b.st[0] = nloc; b.st[1] = nx; }
.Lcv0_end:
.LBB0_680:
	s_cmp_gt_i32 s35, 7
	s_cselect_b64 s[2:3], -1, 0
	s_and_b64 s[0:1], s[0:1], s[2:3]
	s_andn2_b64 vcc, exec, s[0:1]
	s_cbranch_vccnz .LBB0_734
	s_waitcnt vmcnt(0)
	s_waitcnt vmcnt(0) lgkmcnt(0)
	s_barrier
	s_and_saveexec_b64 s[0:1], s[6:7]
	s_cbranch_execz .LBB0_733
	s_add_i32 s4, 0, 0x20160
	v_mov_b32_e32 v1, s4
	s_waitcnt vmcnt(0) expcnt(0) lgkmcnt(0)
	ds_read_b32 v3, v1
	s_add_i32 s4, 0, 0x20164
	v_mov_b32_e32 v1, s4
	ds_read_b32 v1, v1
	s_waitcnt lgkmcnt(1)
	v_cmp_ne_u32_e32 vcc, 0, v3
	s_cbranch_vccnz .LBB0_697
	s_load_dwordx2 s[12:13], s[92:93], 0x4
	s_add_u32 s4, s26, 0x4200
	s_addc_u32 s5, s27, 0
	s_add_u32 s10, s26, 0x4400
	s_addc_u32 s11, s27, 0
	s_waitcnt lgkmcnt(0)
	s_mul_i32 s9, s12, s67
	s_add_u32 s12, s26, 0x4500
	s_mul_i32 s9, s9, s13
	s_addc_u32 s13, s27, 0
	s_add_u32 s14, s26, 0x4600
	s_addc_u32 s15, s27, 0
	s_add_u32 s16, s26, 0x4700
	s_addc_u32 s17, s27, 0
	s_add_u32 s18, s26, 0x4800
	s_addc_u32 s19, s27, 0
	s_add_u32 s20, s26, 0x4900
	s_addc_u32 s21, s27, 0
	s_add_u32 s22, s26, 0x4a00
	s_addc_u32 s23, s27, 0
	s_add_u32 s40, s26, 0x4b00
	s_addc_u32 s41, s27, 0
	s_add_u32 s42, s26, 0x4c00
	s_addc_u32 s43, s27, 0
	s_add_u32 s44, s26, 0x4d00
	s_addc_u32 s45, s27, 0
	s_add_u32 s46, s26, 0x4e00
	s_addc_u32 s47, s27, 0
	s_add_u32 s48, s26, 0x4f00
	s_addc_u32 s49, s27, 0
	s_add_u32 s50, s26, 0x5000
	s_addc_u32 s51, s27, 0
	s_add_u32 s52, s26, 0x5100
	s_addc_u32 s53, s27, 0
	s_add_u32 s54, s26, 0x5200
	s_addc_u32 s55, s27, 0
	s_add_u32 s56, s26, 0x5300
	s_addc_u32 s57, s27, 0
	s_mov_b32 s64, 1
	v_mov_b32_e32 v17, 0
	s_branch .LBB0_685
